# adds scan-A step-8: one GL read instead of four masked ones on diagonal tiles; wave-0 deferred products read both fragment pairs before waiting
# speedup vs baseline: 1.0084x; 1.0048x over previous
; DI void phase_scan_a(Frame& F, int l, int u_lo, int u_hi, int u_step) {
;     ...
;         { const LAS unsigned char* yb = (wave < 4) ? MB(4) : MB(2); LAS unsigned char* ob = (wave < 4) ? MB(3) : MB(0);
;           const int tm = wave & 3, ysw = (wave < 4) ? 3 : 0;
;           bf16x8 xf[2], yf[4][2]; int lq = lane; asm volatile("" : "+v"(lq));
; #pragma unroll
;           for (int s = 0; s < 2; ++s) { xf[s] = mfrag(MB(11), MP, 16 * tm, s, 0, lq);
; #pragma unroll
;               for (int n = 0; n < 4; ++n) yf[n][s] = mfrag(yb, MP, 16 * n, s, ysw, lq); }
;           PIN8(xf[0]); PIN8(xf[1]);
; #pragma unroll
;           for (int n = 0; n < 4; ++n) { PIN8(yf[n][0]); PIN8(yf[n][1]); }
; #pragma unroll
;           for (int tn = 0; tn < 4; ++tn) { f32x4 acc = {0.f, 0.f, 0.f, 0.f};
;               acc = mfma16(xf[0], yf[tn][0], acc); acc = mfma16(xf[1], yf[tn][1], acc);
;               *(LAS u32x2*)(ob + (16 * tn + r16) * MP + (16 * tm + 4 * g) * 2) = pk4(acc); } }
;         __syncthreads();
;         }
;     ...
;         asm volatile("" : "+v"(plw[0]), "+v"(plw[1]), "+v"(plw[2]), "+v"(plw[3]), "+v"(plw[4]), "+v"(plw[5]), "+v"(plw[6]), "+v"(plw[7]), "+v"(prv), "+v"(pkv), "+v"(pav), "+v"(pbv), "+v"(pvv));
;     ...
;         SA_REP(16) {
;         { const int tm = wave >> 1;
;           bf16x8 x3[2], x0[2], x6[2], y9[2][2], y6[2][2], y0[2][2]; u32x2 rrv[2]; int lq = lane; asm volatile("" : "+v"(lq));
; #pragma unroll
;           for (int s = 0; s < 2; ++s) { x3[s] = mfrag(MB(3), MP, 16 * tm, s, 0, lq); x0[s] = mfrag(MB(0), MP, 16 * tm, s, 0, lq); x6[s] = mfrag(MB(6), MP, 16 * tm, s, 3, lq);
; #pragma unroll
;               for (int q = 0; q < 2; ++q) { const int tn = (wave * 2 + q) & 3; y9[q][s] = mfrag(MB(9), MP, 16 * tn, s, 0, lq); y6[q][s] = mfrag(MB(6), MP, 16 * tn, s, 3, lq); y0[q][s] = mfrag(MB(0), MP, 16 * tn, s, 0, lq); } }
; #pragma unroll
;           for (int q = 0; q < 2; ++q) { const int tn = (wave * 2 + q) & 3; rrv[q] = *(const LAS u32x2*)(MB(1) + (16 * tn + r16) * MP + (16 * tm + 4 * g) * 2); }
;           PIN8(x3[0]); PIN8(x3[1]); PIN8(x0[0]); PIN8(x0[1]); PIN8(x6[0]); PIN8(x6[1]);
; #pragma unroll
;           for (int q = 0; q < 2; ++q) { PIN8(y9[q][0]); PIN8(y9[q][1]); PIN8(y6[q][0]); PIN8(y6[q][1]); PIN8(y0[q][0]); PIN8(y0[q][1]); PIN8(rrv[q]); }
; #pragma unroll
;           for (int q = 0; q < 2; ++q) { const int tn = (wave * 2 + q) & 3;
.LBB0_1140:
	v_mov_b32_e32 v36, v210
	s_waitcnt lgkmcnt(0)
	s_barrier
	v_readlane_b32 s42, v255, 41
	v_and_b32_e32 v37, 15, v36
	s_movk_i32 s60, 0x90
	v_or_b32_e32 v39, s42, v37
	v_readlane_b32 s42, v255, 11
	v_lshrrev_b32_e32 v38, 4, v36
	v_and_b32_e32 v36, -16, v36
	v_mov_b32_e32 v40, s42
	v_readlane_b32 s42, v255, 40
	v_mad_u32_u24 v39, v39, s60, v40
	v_readlane_b32 s43, v254, 5
	v_mov_b32_e32 v40, s42
	v_mad_u32_u24 v37, v37, s60, v40
	v_readlane_b32 s42, v254, 4
	v_add_u32_e32 v40, v39, v36
	v_add_u32_e32 v41, v37, v36
	v_xor_b32_e32 v36, s42, v38
	v_lshl_add_u32 v52, v36, 4, v37
	v_xor_b32_e32 v36, s43, v38
	v_readlane_b32 s56, v254, 6
	v_lshl_add_u32 v56, v36, 4, v37
	s_ashr_i32 s40, s62, 5
	v_xor_b32_e32 v36, s56, v38
	v_lshl_add_u32 v66, v36, 4, v37
	v_add_u32_e32 v36, 4, v38
	v_lshlrev_b32_e32 v38, 4, v36
	v_add_u32_e32 v60, v39, v38
	v_add_u32_e32 v44, v37, v38
	v_xor_b32_e32 v38, s42, v36
	v_lshl_add_u32 v48, v38, 4, v37
	v_xor_b32_e32 v38, s43, v36
	v_xor_b32_e32 v36, s56, v36
	v_lshl_add_u32 v70, v38, 4, v37
	v_lshl_add_u32 v74, v36, 4, v37
	ds_read_b128 v[36:39], v40
	ds_read_b128 v[40:43], v41
	ds_read_b128 v[44:47], v44
	ds_read_b128 v[48:51], v48 offset:2304
	ds_read_b128 v[52:55], v52 offset:2304
	ds_read_b128 v[56:59], v56 offset:4608
	ds_read_b128 v[60:63], v60
	ds_read_b128 v[66:69], v66 offset:6912
	ds_read_b128 v[70:73], v70 offset:4608
	ds_read_b128 v[74:77], v74 offset:6912
	s_waitcnt lgkmcnt(9)
	s_waitcnt lgkmcnt(3)
	s_waitcnt lgkmcnt(1)
	v_mfma_f32_16x16x32_bf16 v[40:43], v[36:39], v[40:43], 0
	s_waitcnt lgkmcnt(0)
	s_and_b32 s41, s66, 0xf80
	v_mfma_f32_16x16x32_bf16 v[40:43], v[60:63], v[44:47], v[40:43]
	s_add_i32 s40, s41, s40
	s_ashr_i32 s41, s40, 31
	s_lshl_b64 s[58:59], s[40:41], 14
	v_mfma_f32_16x16x32_bf16 v[44:47], v[36:39], v[52:55], 0
	v_readlane_b32 s40, v255, 17
	s_nop 2
	v_cvt_pk_bf16_f32 v40, v40, v41
	v_cvt_pk_bf16_f32 v41, v42, v43
	v_mfma_f32_16x16x32_bf16 v[44:47], v[60:63], v[48:51], v[44:47]
	ds_write_b64 v207, v[40:41]
	s_add_u32 s42, s40, s58
	v_readlane_b32 s40, v255, 18
	v_mfma_f32_16x16x32_bf16 v[48:51], v[36:39], v[56:59], 0
	s_addc_u32 s43, s40, s59
	s_nop 2
	v_cvt_pk_bf16_f32 v44, v44, v45
	v_cvt_pk_bf16_f32 v45, v46, v47
	v_mfma_f32_16x16x32_bf16 v[36:39], v[36:39], v[66:69], 0
	ds_write_b64 v207, v[44:45] offset:2304
	v_readlane_b32 s40, v255, 33
	v_readlane_b32 s41, v255, 13
	v_mfma_f32_16x16x32_bf16 v[36:39], v[60:63], v[74:77], v[36:39]
	v_readlane_b32 vcc_lo, v254, 7
	s_mov_b32 s70, s61
	v_mov_b32_e32 v45, s69
	v_mfma_f32_16x16x32_bf16 v[40:43], v[60:63], v[70:73], v[48:51]
	s_add_u32 s56, s42, 0x2000
	s_nop 2
	v_cvt_pk_bf16_f32 v36, v36, v37
	v_cvt_pk_bf16_f32 v37, v38, v39
	ds_write_b64 v207, v[36:37] offset:6912
	v_mov_b32_e32 v36, v210
	v_cvt_pk_bf16_f32 v40, v40, v41
	v_cvt_pk_bf16_f32 v41, v42, v43
	ds_write_b64 v207, v[40:41] offset:4608
	s_waitcnt lgkmcnt(0)
	s_barrier
	s_waitcnt vmcnt(0)
	s_addc_u32 s57, s43, 0
	v_and_b32_e32 v37, 15, v36
	v_or_b32_e32 v39, s40, v37
	v_mul_lo_u32 v39, v39, s60
	s_mov_b32 s40, s69
	v_lshrrev_b32_e32 v38, 4, v36
	v_add_u32_e32 v39, s40, v39
	v_and_b32_e32 v36, -16, v36
	v_or_b32_e32 v40, s61, v37
	v_add_u32_e32 v41, v39, v36
	v_add_u32_e32 v43, s41, v36
	v_add_u32_e32 v36, s40, v36
	v_or_b32_e32 v37, vcc_lo, v37
	v_readlane_b32 s61, v255, 42
	v_mad_u32_u24 v48, v40, s60, v36
	v_mad_u32_u24 v50, v37, s60, v36
	v_add_u32_e32 v36, 4, v38
	v_xor_b32_e32 v42, s61, v38
	v_mad_u32_u24 v44, v40, s60, v43
	v_mad_u32_u24 v46, v40, s60, v45
	v_xor_b32_e32 v47, s33, v38
	v_mad_u32_u24 v49, v37, s60, v43
	v_mad_u32_u24 v43, v37, s60, v45
	v_xor_b32_e32 v45, s44, v38
	v_lshlrev_b32_e32 v38, 4, v36
	v_xor_b32_e32 v52, s61, v36
	v_lshl_add_u32 v42, v42, 4, v39
	v_add_u32_e32 v51, v39, v38
	v_lshl_add_u32 v39, v52, 4, v39
	v_add_u32_e32 v52, s41, v38
	v_add_u32_e32 v38, s40, v38
	v_xor_b32_e32 v53, s33, v36
	v_xor_b32_e32 v36, s44, v36
	v_lshl_add_u32 v47, v47, 4, v46
	v_lshl_add_u32 v45, v45, 4, v43
	v_mad_u32_u24 v56, v40, s60, v52
	v_lshl_add_u32 v46, v53, 4, v46
	v_mad_u32_u24 v57, v40, s60, v38
	v_mad_u32_u24 v58, v37, s60, v52
	v_lshl_add_u32 v78, v36, 4, v43
	v_mad_u32_u24 v225, v37, s60, v38
	ds_read_b64 v[222:223], v208 offset:9216
	ds_read_b64 v[126:127], v209 offset:9216
	ds_read_b128 v[74:77], v41 offset:27648
	ds_read_b128 v[52:55], v41
	ds_read_b128 v[70:73], v51 offset:27648
	ds_read_b128 v[36:39], v39 offset:55296
	ds_read_b128 v[40:43], v42 offset:55296
	ds_read_b128 v[98:101], v44
	ds_read_b128 v[94:97], v56
	ds_read_b128 v[102:105], v46 offset:55296
	ds_read_b128 v[202:205], v47 offset:55296
	ds_read_b128 v[86:89], v48
	ds_read_b128 v[90:93], v57
	ds_read_b128 v[56:59], v58
	ds_read_b128 v[60:63], v49
	ds_read_b128 v[82:85], v45 offset:55296
	ds_read_b128 v[66:69], v51
	ds_read_b128 v[44:47], v50
	ds_read_b128 v[78:81], v78 offset:55296
	ds_read_b128 v[48:51], v225
	s_waitcnt lgkmcnt(14)
	s_waitcnt lgkmcnt(3)
	s_nop 0
	v_mfma_f32_16x16x32_bf16 v[226:229], v[74:77], v[98:101], 0
	v_mfma_f32_16x16x32_bf16 v[202:205], v[74:77], v[202:205], 0
	v_lshlrev_b32_e32 v234, 16, v222
	v_and_b32_e32 v235, 0xffff0000, v222
	v_lshlrev_b32_e32 v222, 16, v223
	v_mfma_f32_16x16x32_bf16 v[226:229], v[70:73], v[94:97], v[226:229]
	v_and_b32_e32 v223, 0xffff0000, v223
	s_waitcnt lgkmcnt(1)
	v_mfma_f32_16x16x32_bf16 v[102:105], v[70:73], v[102:105], v[202:205]
	s_nop 4
	v_add_f32_e64 v226, v226, v234
	v_add_f32_e64 v227, v227, v235
	v_pk_add_f32 v[222:223], v[228:229], v[222:223]
	v_cvt_pk_bf16_f32 v226, v226, v227
	v_cvt_pk_bf16_f32 v227, v222, v223
	v_lshl_add_u64 v[222:223], s[56:57], 0, v[114:115]
	s_waitcnt lgkmcnt(0)
	global_store_dwordx2 v[222:223], v[226:227], off
	s_or_b64 s[40:41], s[92:93], s[94:95]
	s_or_b64 s[40:41], s[40:41], s[96:97]
	s_or_b64 s[40:41], s[40:41], s[4:5]
	s_and_b64 s[40:41], s[40:41], exec
	s_cbranch_scc0 .Lsa8_g1_done
	ds_read_b32 v202, v184
	s_mov_b64 s[40:41], exec
	s_waitcnt lgkmcnt(0)
	s_and_b64 exec, s[40:41], s[92:93]
	v_add_f32_e32 v102, v102, v202
	s_and_b64 exec, s[40:41], s[94:95]
	v_add_f32_e32 v103, v103, v202
	s_and_b64 exec, s[40:41], s[96:97]
	v_add_f32_e32 v104, v104, v202
	s_and_b64 exec, s[40:41], s[4:5]
	v_add_f32_e32 v105, v105, v202
	s_mov_b64 exec, s[40:41]
.Lsa8_g1_done:
	s_branch .Lsa8_g1_join
.LBB0_1144:
	s_andn2_b64 vcc, exec, s[56:57]
	s_cbranch_vccnz .LBB0_1106

; DI float bflo(unsigned w) { return __uint_as_float(w << 16); }
; DI float bfhi(unsigned w) { return __uint_as_float(w & 0xffff0000u); }
; DI f32x4 mfma16(bf16x8 a, bf16x8 b, f32x4 c) { return __builtin_amdgcn_mfma_f32_16x16x32_bf16(a, b, c, 0, 0, 0); }
; DI int permk(int k) { return (k & 32) | (((k >> 2) & 3) << 3) | (((k >> 4) & 1) << 2) | (k & 3); }
; DI u32x2 pk4(f32x4 v) { u32x2 w; w.x = pk2(v[0], v[1]); w.y = pk2(v[2], v[3]); return w; }
; DI void phase_scan_a(Frame& F, int l, int u_lo, int u_hi, int u_step) {
;     ...
;           for (int q = 0; q < 2; ++q) { const int tn = (wave * 2 + q) & 3;
;             { f32x4 acc = {0.f, 0.f, 0.f, 0.f}; acc = mfma16(x3[0], y9[q][0], acc); acc = mfma16(x3[1], y9[q][1], acc);
;               const int i = 16 * tn + r16, k0 = 16 * tm + 4 * g; const u32x2 rr = rrv[q];
;               acc[0] += bflo(rr.x); acc[1] += bfhi(rr.x); acc[2] += bflo(rr.y); acc[3] += bfhi(rr.y);
;               *(u32x2*)(rec1 + U_RPP + (size_t)(i * 64 + permk(k0)) * 2) = pk4(acc); }
;             { f32x4 acc = {0.f, 0.f, 0.f, 0.f}; acc = mfma16(x3[0], y6[q][0], acc); acc = mfma16(x3[1], y6[q][1], acc);
;               const int kp = 16 * tn + r16, k0 = 16 * tm + 4 * g;
; #pragma unroll
;               for (int r = 0; r < 4; ++r) if (k0 + r == kp) acc[r] += GL[kp];
;               *(u32x2*)(rec1 + U_PMP + (size_t)(kp * 64 + permk(k0)) * 2) = pk4(acc); }
;             { f32x4 acc = pyl[q]; acc = mfma16(x0[0], y9[q][0], acc); acc = mfma16(x0[1], y9[q][1], acc); if (wave == 0) acc = mm_tile(MB(5), MP, 16 * tm, MB(10), MP, 16 * tn, 2, acc, lane, 3, 0);
;               *(u32x2*)(rec2 + U_YLT + (size_t)((16 * tn + r16) * 64 + 16 * tm + 4 * g) * 2) = pk4(acc); }
;             { f32x4 acc = pqm[q]; acc = mfma16(x6[0], y0[q][0], acc); acc = mfma16(x6[1], y0[q][1], acc); if (wave == 0) acc = mm_tile(MB(7), MP, 16 * tm, MB(5), MP, 16 * tn, 2, acc, lane, 3, 3);
;               *(u32x2*)(rec2 + U_QMT + (size_t)((16 * tn + r16) * 64 + 16 * tm + 4 * g) * 2) = pk4(acc); }
.Lsa8_g1_join:
	v_mfma_f32_16x16x32_bf16 v[32:35], v[52:55], v[98:101], v[32:35]
	v_readlane_b32 s60, v255, 26
	v_readlane_b32 s61, v255, 27
	v_cvt_pk_bf16_f32 v102, v102, v103
	v_mfma_f32_16x16x32_bf16 v[32:35], v[66:69], v[94:97], v[32:35]
	v_cndmask_b32_e64 v98, 0, 1, s[60:61]
	v_cvt_pk_bf16_f32 v103, v104, v105
	v_lshl_add_u64 v[104:105], s[42:43], 0, v[114:115]
	v_cmp_ne_u32_e64 s[40:41], 1, v98
	s_andn2_b64 vcc, exec, s[60:61]
	global_store_dwordx2 v[104:105], v[102:103], off
	s_cbranch_vccnz .LBB0_1154
	ds_read_b128 v[94:97], v221 offset:46080
	ds_read_b128 v[98:101], v216
	ds_read_b128 v[236:239], v221 offset:46144
	ds_read_b128 v[240:243], v216 offset:64
	s_waitcnt lgkmcnt(2)
	v_mfma_f32_16x16x32_bf16 v[32:35], v[94:97], v[98:101], v[32:35]
	s_waitcnt lgkmcnt(0)
	v_mfma_f32_16x16x32_bf16 v[32:35], v[236:239], v[240:243], v[32:35]
.LBB0_1154:
	v_mfma_f32_16x16x32_bf16 v[28:31], v[40:43], v[86:89], v[28:31]
	v_readlane_b32 s60, v255, 15
	s_add_u32 s58, s60, s58
	v_readlane_b32 s60, v255, 16
	s_addc_u32 s59, s60, s59
	v_mfma_f32_16x16x32_bf16 v[28:31], v[36:39], v[90:93], v[28:31]
	s_add_u32 s60, s58, 0x2000
	s_addc_u32 s61, s59, 0
	v_cvt_pk_bf16_f32 v32, v32, v33
	v_cvt_pk_bf16_f32 v33, v34, v35
	v_lshl_add_u64 v[34:35], s[60:61], 0, v[116:117]
	s_and_b64 vcc, exec, s[40:41]
	global_store_dwordx2 v[34:35], v[32:33], off
	s_cbranch_vccnz .LBB0_1156
	ds_read_b128 v[32:35], v221 offset:64512
	ds_read_b128 v[86:89], v217 offset:46080
	ds_read_b128 v[236:239], v221 offset:64576
	ds_read_b128 v[240:243], v217 offset:46144
	s_waitcnt lgkmcnt(2)
	v_mfma_f32_16x16x32_bf16 v[28:31], v[32:35], v[86:89], v[28:31]
	s_waitcnt lgkmcnt(0)
	v_mfma_f32_16x16x32_bf16 v[28:31], v[236:239], v[240:243], v[28:31]
.LBB0_1156:
	s_nop 7
	v_cvt_pk_bf16_f32 v28, v28, v29
	v_cvt_pk_bf16_f32 v29, v30, v31
	v_lshl_add_u64 v[30:31], s[58:59], 0, v[116:117]
	global_store_dwordx2 v[30:31], v[28:29], off
	v_mfma_f32_16x16x32_bf16 v[28:31], v[74:77], v[60:63], 0
	v_lshlrev_b32_e32 v32, 16, v126
	v_and_b32_e32 v33, 0xffff0000, v126
	v_mfma_f32_16x16x32_bf16 v[28:31], v[70:73], v[56:59], v[28:31]
	s_nop 7
	v_pk_add_f32 v[28:29], v[28:29], v[32:33]
	v_lshlrev_b32_e32 v32, 16, v127
	v_and_b32_e32 v33, 0xffff0000, v127
	v_pk_add_f32 v[30:31], v[30:31], v[32:33]
	v_cvt_pk_bf16_f32 v28, v28, v29
	v_cvt_pk_bf16_f32 v29, v30, v31
	v_lshl_add_u64 v[30:31], s[56:57], 0, v[118:119]
	global_store_dwordx2 v[30:31], v[28:29], off
	v_mfma_f32_16x16x32_bf16 v[28:31], v[74:77], v[82:85], 0
	v_mfma_f32_16x16x32_bf16 v[28:31], v[70:73], v[78:81], v[28:31]
	s_or_b64 s[56:57], s[6:7], s[10:11]
	s_or_b64 s[56:57], s[56:57], s[2:3]
	s_or_b64 s[56:57], s[56:57], s[0:1]
	s_and_b64 s[56:57], s[56:57], exec
	s_cbranch_scc0 .Lsa8_g2_done
	ds_read_b32 v32, v185
	s_mov_b64 s[56:57], exec
	s_waitcnt lgkmcnt(0)
	s_and_b64 exec, s[56:57], s[6:7]
	v_add_f32_e32 v28, v28, v32
	s_and_b64 exec, s[56:57], s[10:11]
	v_add_f32_e32 v29, v29, v32
	s_and_b64 exec, s[56:57], s[2:3]
	v_add_f32_e32 v30, v30, v32
	s_and_b64 exec, s[56:57], s[0:1]
	v_add_f32_e32 v31, v31, v32
	s_mov_b64 exec, s[56:57]
.Lsa8_g2_done:
	s_nop 3
	v_mfma_f32_16x16x32_bf16 v[24:27], v[52:55], v[60:63], v[24:27]
	v_cvt_pk_bf16_f32 v28, v28, v29
	v_cvt_pk_bf16_f32 v29, v30, v31
	v_lshl_add_u64 v[30:31], s[42:43], 0, v[118:119]
	v_mfma_f32_16x16x32_bf16 v[24:27], v[66:69], v[56:59], v[24:27]
	s_and_b64 vcc, exec, s[40:41]
	global_store_dwordx2 v[30:31], v[28:29], off
	s_cbranch_vccnz .LBB0_1166
	ds_read_b128 v[28:31], v221 offset:46080
	ds_read_b128 v[32:35], v218
	ds_read_b128 v[236:239], v221 offset:46144
	ds_read_b128 v[240:243], v218 offset:64
	s_waitcnt lgkmcnt(2)
	v_mfma_f32_16x16x32_bf16 v[24:27], v[28:31], v[32:35], v[24:27]
	s_waitcnt lgkmcnt(0)
	v_mfma_f32_16x16x32_bf16 v[24:27], v[236:239], v[240:243], v[24:27]
.LBB0_1166:
	v_mfma_f32_16x16x32_bf16 v[20:23], v[40:43], v[44:47], v[20:23]
	s_nop 6
	v_cvt_pk_bf16_f32 v24, v24, v25
	v_cvt_pk_bf16_f32 v25, v26, v27
	v_lshl_add_u64 v[26:27], s[60:61], 0, v[120:121]
	v_mfma_f32_16x16x32_bf16 v[20:23], v[36:39], v[48:51], v[20:23]
	s_and_b64 vcc, exec, s[40:41]
	global_store_dwordx2 v[26:27], v[24:25], off
	s_cbranch_vccnz .LBB0_1013
	ds_read_b128 v[24:27], v221 offset:64512
	ds_read_b128 v[28:31], v219 offset:46080
	ds_read_b128 v[236:239], v221 offset:64576
	ds_read_b128 v[240:243], v220 offset:46080
	s_waitcnt lgkmcnt(2)
	v_mfma_f32_16x16x32_bf16 v[20:23], v[24:27], v[28:31], v[20:23]
	s_waitcnt lgkmcnt(0)
	v_mfma_f32_16x16x32_bf16 v[20:23], v[236:239], v[240:243], v[20:23]
	s_branch .LBB0_1013
